# e6
# speedup vs baseline: 1.0298x; 1.0033x over previous
.LBB12_3:
	s_or_b64 exec, exec, s[4:5]
	v_mov_b32_e32 v2, 2
	v_lshlrev_b32_sdwa v2, v2, v0 dst_sel:DWORD dst_unused:UNUSED_PAD src0_sel:DWORD src1_sel:BYTE_0
	v_lshl_or_b32 v16, v1, 16, v2
	v_mov_b32_e32 v3, 0
	v_lshlrev_b32_e32 v24, 8, v1
	v_add_u32_e32 v23, 64, v22
	v_or_b32_e32 v2, 0x3c00, v16
	v_or_b32_e32 v4, 0x3400, v16
	v_mov_b32_e32 v5, v3
	v_or_b32_e32 v25, 0x2000, v24
	v_or_b32_e32 v6, 0x2c00, v16
	v_mov_b32_e32 v7, v3
	v_or_b32_e32 v8, 0x400, v16
	v_mov_b32_e32 v9, v3
	v_or_b32_e32 v10, 0x2400, v16
	v_mov_b32_e32 v11, v3
	v_or_b32_e32 v12, 0x1c00, v16
	v_mov_b32_e32 v13, v3
	v_or_b32_e32 v14, 0xc00, v16
	v_mov_b32_e32 v15, v3
	v_or_b32_e32 v16, 0x1400, v16
	v_mov_b32_e32 v17, v3
	s_mov_b64 s[4:5], 0
	s_waitcnt lgkmcnt(0)
	s_mov_b64 s[20:21], s[8:9]
	v_mov_b32_e32 v26, v22
	v_mov_b32_e32 v18, v3
	v_mov_b32_e32 v19, v3
	v_mov_b32_e32 v20, v3
	v_mov_b32_e32 v21, v3
	s_barrier
	v_lshl_add_u64 v[28:29], s[20:21], 0, v[8:9]
	v_lshl_add_u64 v[30:31], s[20:21], 0, v[14:15]
	v_lshl_add_u64 v[32:33], s[20:21], 0, v[16:17]
	v_lshl_add_u64 v[34:35], s[20:21], 0, v[12:13]
	v_lshl_add_u64 v[36:37], s[20:21], 0, v[10:11]
	v_lshl_add_u64 v[38:39], s[20:21], 0, v[6:7]
	v_lshl_add_u64 v[40:41], s[20:21], 0, v[4:5]
	v_lshl_add_u64 v[42:43], s[20:21], 0, v[2:3]
	global_load_dword v56, v[28:29], off offset:-1024
	global_load_dword v57, v[28:29], off
	global_load_dword v58, v[30:31], off offset:-1024
	global_load_dword v59, v[30:31], off
	global_load_dword v60, v[32:33], off offset:-1024
	global_load_dword v61, v[32:33], off
	global_load_dword v62, v[34:35], off offset:-1024
	global_load_dword v63, v[34:35], off
	global_load_dword v64, v[36:37], off offset:-1024
	global_load_dword v65, v[36:37], off
	global_load_dword v66, v[38:39], off offset:-1024
	global_load_dword v67, v[38:39], off
	global_load_dword v68, v[40:41], off offset:-1024
	global_load_dword v69, v[40:41], off
	global_load_dword v70, v[42:43], off offset:-1024
	global_load_dword v71, v[42:43], off
	s_add_u32 s20, s20, 0x4000
	s_addc_u32 s21, s21, 0
	v_lshl_add_u64 v[28:29], s[20:21], 0, v[8:9]
	v_lshl_add_u64 v[30:31], s[20:21], 0, v[14:15]
	v_lshl_add_u64 v[32:33], s[20:21], 0, v[16:17]
	v_lshl_add_u64 v[34:35], s[20:21], 0, v[12:13]
	v_lshl_add_u64 v[36:37], s[20:21], 0, v[10:11]
	v_lshl_add_u64 v[38:39], s[20:21], 0, v[6:7]
	v_lshl_add_u64 v[40:41], s[20:21], 0, v[4:5]
	v_lshl_add_u64 v[42:43], s[20:21], 0, v[2:3]
	global_load_dword v72, v[28:29], off offset:-1024
	global_load_dword v73, v[28:29], off
	global_load_dword v74, v[30:31], off offset:-1024
	global_load_dword v75, v[30:31], off
	global_load_dword v76, v[32:33], off offset:-1024
	global_load_dword v77, v[32:33], off
	global_load_dword v78, v[34:35], off offset:-1024
	global_load_dword v79, v[34:35], off
	global_load_dword v80, v[36:37], off offset:-1024
	global_load_dword v81, v[36:37], off
	global_load_dword v82, v[38:39], off offset:-1024
	global_load_dword v83, v[38:39], off
	global_load_dword v84, v[40:41], off offset:-1024
	global_load_dword v85, v[40:41], off
	global_load_dword v86, v[42:43], off offset:-1024
	global_load_dword v87, v[42:43], off
	s_add_u32 s20, s20, 0x4000
	s_addc_u32 s21, s21, 0
	v_lshl_add_u64 v[28:29], s[20:21], 0, v[8:9]
	v_lshl_add_u64 v[30:31], s[20:21], 0, v[14:15]
	v_lshl_add_u64 v[32:33], s[20:21], 0, v[16:17]
	v_lshl_add_u64 v[34:35], s[20:21], 0, v[12:13]
	v_lshl_add_u64 v[36:37], s[20:21], 0, v[10:11]
	v_lshl_add_u64 v[38:39], s[20:21], 0, v[6:7]
	v_lshl_add_u64 v[40:41], s[20:21], 0, v[4:5]
	v_lshl_add_u64 v[42:43], s[20:21], 0, v[2:3]
	global_load_dword v88, v[28:29], off offset:-1024
	global_load_dword v89, v[28:29], off
	global_load_dword v90, v[30:31], off offset:-1024
	global_load_dword v91, v[30:31], off
	global_load_dword v92, v[32:33], off offset:-1024
	global_load_dword v93, v[32:33], off
	global_load_dword v94, v[34:35], off offset:-1024
	global_load_dword v95, v[34:35], off
	global_load_dword v96, v[36:37], off offset:-1024
	global_load_dword v97, v[36:37], off
	global_load_dword v98, v[38:39], off offset:-1024
	global_load_dword v99, v[38:39], off
	global_load_dword v100, v[40:41], off offset:-1024
	global_load_dword v101, v[40:41], off
	global_load_dword v102, v[42:43], off offset:-1024
	global_load_dword v103, v[42:43], off
	s_add_u32 s20, s20, 0x4000
	s_addc_u32 s21, s21, 0
	ds_read_b128 v[28:31], v25 offset:0
	ds_read_b128 v[32:35], v25 offset:16
	ds_read_b128 v[36:39], v25 offset:32
	ds_read_b128 v[40:43], v25 offset:48
	ds_read_b128 v[44:47], v25 offset:1024
	ds_read_b128 v[48:51], v25 offset:1040
	ds_read_b128 v[52:55], v25 offset:1056
	ds_read_b128 v[120:123], v25 offset:1072
	s_waitcnt vmcnt(32) lgkmcnt(0)
	v_pk_fma_f32 v[20:21], v[56:57], v[28:29], v[20:21]
	v_pk_fma_f32 v[18:19], v[56:57], v[44:45], v[18:19]
	v_pk_fma_f32 v[20:21], v[58:59], v[30:31], v[20:21]
	v_pk_fma_f32 v[18:19], v[58:59], v[46:47], v[18:19]
	v_pk_fma_f32 v[20:21], v[60:61], v[32:33], v[20:21]
	v_pk_fma_f32 v[18:19], v[60:61], v[48:49], v[18:19]
	v_pk_fma_f32 v[20:21], v[62:63], v[34:35], v[20:21]
	v_pk_fma_f32 v[18:19], v[62:63], v[50:51], v[18:19]
	v_pk_fma_f32 v[20:21], v[64:65], v[36:37], v[20:21]
	v_pk_fma_f32 v[18:19], v[64:65], v[52:53], v[18:19]
	v_pk_fma_f32 v[20:21], v[66:67], v[38:39], v[20:21]
	v_pk_fma_f32 v[18:19], v[66:67], v[54:55], v[18:19]
	v_pk_fma_f32 v[20:21], v[68:69], v[40:41], v[20:21]
	v_pk_fma_f32 v[18:19], v[68:69], v[120:121], v[18:19]
	v_pk_fma_f32 v[20:21], v[70:71], v[42:43], v[20:21]
	v_pk_fma_f32 v[18:19], v[70:71], v[122:123], v[18:19]
	v_lshl_add_u64 v[28:29], s[20:21], 0, v[8:9]
	v_lshl_add_u64 v[30:31], s[20:21], 0, v[14:15]
	v_lshl_add_u64 v[32:33], s[20:21], 0, v[16:17]
	v_lshl_add_u64 v[34:35], s[20:21], 0, v[12:13]
	v_lshl_add_u64 v[36:37], s[20:21], 0, v[10:11]
	v_lshl_add_u64 v[38:39], s[20:21], 0, v[6:7]
	v_lshl_add_u64 v[40:41], s[20:21], 0, v[4:5]
	v_lshl_add_u64 v[42:43], s[20:21], 0, v[2:3]
	global_load_dword v104, v[28:29], off offset:-1024
	global_load_dword v105, v[28:29], off
	global_load_dword v106, v[30:31], off offset:-1024
	global_load_dword v107, v[30:31], off
	global_load_dword v108, v[32:33], off offset:-1024
	global_load_dword v109, v[32:33], off
	global_load_dword v110, v[34:35], off offset:-1024
	global_load_dword v111, v[34:35], off
	global_load_dword v112, v[36:37], off offset:-1024
	global_load_dword v113, v[36:37], off
	global_load_dword v114, v[38:39], off offset:-1024
	global_load_dword v115, v[38:39], off
	global_load_dword v116, v[40:41], off offset:-1024
	global_load_dword v117, v[40:41], off
	global_load_dword v118, v[42:43], off offset:-1024
	global_load_dword v119, v[42:43], off
	s_add_u32 s20, s20, 0x4000
	s_addc_u32 s21, s21, 0
	ds_read_b128 v[28:31], v25 offset:64
	ds_read_b128 v[32:35], v25 offset:80
	ds_read_b128 v[36:39], v25 offset:96
	ds_read_b128 v[40:43], v25 offset:112
	ds_read_b128 v[44:47], v25 offset:1088
	ds_read_b128 v[48:51], v25 offset:1104
	ds_read_b128 v[52:55], v25 offset:1120
	ds_read_b128 v[120:123], v25 offset:1136
	s_waitcnt vmcnt(32) lgkmcnt(0)
	v_pk_fma_f32 v[20:21], v[72:73], v[28:29], v[20:21]
	v_pk_fma_f32 v[18:19], v[72:73], v[44:45], v[18:19]
	v_pk_fma_f32 v[20:21], v[74:75], v[30:31], v[20:21]
	v_pk_fma_f32 v[18:19], v[74:75], v[46:47], v[18:19]
	v_pk_fma_f32 v[20:21], v[76:77], v[32:33], v[20:21]
	v_pk_fma_f32 v[18:19], v[76:77], v[48:49], v[18:19]
	v_pk_fma_f32 v[20:21], v[78:79], v[34:35], v[20:21]
	v_pk_fma_f32 v[18:19], v[78:79], v[50:51], v[18:19]
	v_pk_fma_f32 v[20:21], v[80:81], v[36:37], v[20:21]
	v_pk_fma_f32 v[18:19], v[80:81], v[52:53], v[18:19]
	v_pk_fma_f32 v[20:21], v[82:83], v[38:39], v[20:21]
	v_pk_fma_f32 v[18:19], v[82:83], v[54:55], v[18:19]
	v_pk_fma_f32 v[20:21], v[84:85], v[40:41], v[20:21]
	v_pk_fma_f32 v[18:19], v[84:85], v[120:121], v[18:19]
	v_pk_fma_f32 v[20:21], v[86:87], v[42:43], v[20:21]
	v_pk_fma_f32 v[18:19], v[86:87], v[122:123], v[18:19]
	ds_read_b128 v[28:31], v25 offset:128
	ds_read_b128 v[32:35], v25 offset:144
	ds_read_b128 v[36:39], v25 offset:160
	ds_read_b128 v[40:43], v25 offset:176
	ds_read_b128 v[44:47], v25 offset:1152
	ds_read_b128 v[48:51], v25 offset:1168
	ds_read_b128 v[52:55], v25 offset:1184
	ds_read_b128 v[120:123], v25 offset:1200
	s_waitcnt vmcnt(16) lgkmcnt(0)
	v_pk_fma_f32 v[20:21], v[88:89], v[28:29], v[20:21]
	v_pk_fma_f32 v[18:19], v[88:89], v[44:45], v[18:19]
	v_pk_fma_f32 v[20:21], v[90:91], v[30:31], v[20:21]
	v_pk_fma_f32 v[18:19], v[90:91], v[46:47], v[18:19]
	v_pk_fma_f32 v[20:21], v[92:93], v[32:33], v[20:21]
	v_pk_fma_f32 v[18:19], v[92:93], v[48:49], v[18:19]
	v_pk_fma_f32 v[20:21], v[94:95], v[34:35], v[20:21]
	v_pk_fma_f32 v[18:19], v[94:95], v[50:51], v[18:19]
	v_pk_fma_f32 v[20:21], v[96:97], v[36:37], v[20:21]
	v_pk_fma_f32 v[18:19], v[96:97], v[52:53], v[18:19]
	v_pk_fma_f32 v[20:21], v[98:99], v[38:39], v[20:21]
	v_pk_fma_f32 v[18:19], v[98:99], v[54:55], v[18:19]
	v_pk_fma_f32 v[20:21], v[100:101], v[40:41], v[20:21]
	v_pk_fma_f32 v[18:19], v[100:101], v[120:121], v[18:19]
	v_pk_fma_f32 v[20:21], v[102:103], v[42:43], v[20:21]
	v_pk_fma_f32 v[18:19], v[102:103], v[122:123], v[18:19]
	ds_read_b128 v[28:31], v25 offset:192
	ds_read_b128 v[32:35], v25 offset:208
	ds_read_b128 v[36:39], v25 offset:224
	ds_read_b128 v[40:43], v25 offset:240
	ds_read_b128 v[44:47], v25 offset:1216
	ds_read_b128 v[48:51], v25 offset:1232
	ds_read_b128 v[52:55], v25 offset:1248
	ds_read_b128 v[120:123], v25 offset:1264
	s_waitcnt vmcnt(0) lgkmcnt(0)
	v_pk_fma_f32 v[20:21], v[104:105], v[28:29], v[20:21]
	v_pk_fma_f32 v[18:19], v[104:105], v[44:45], v[18:19]
	v_pk_fma_f32 v[20:21], v[106:107], v[30:31], v[20:21]
	v_pk_fma_f32 v[18:19], v[106:107], v[46:47], v[18:19]
	v_pk_fma_f32 v[20:21], v[108:109], v[32:33], v[20:21]
	v_pk_fma_f32 v[18:19], v[108:109], v[48:49], v[18:19]
	v_pk_fma_f32 v[20:21], v[110:111], v[34:35], v[20:21]
	v_pk_fma_f32 v[18:19], v[110:111], v[50:51], v[18:19]
	v_pk_fma_f32 v[20:21], v[112:113], v[36:37], v[20:21]
	v_pk_fma_f32 v[18:19], v[112:113], v[52:53], v[18:19]
	v_pk_fma_f32 v[20:21], v[114:115], v[38:39], v[20:21]
	v_pk_fma_f32 v[18:19], v[114:115], v[54:55], v[18:19]
	v_pk_fma_f32 v[20:21], v[116:117], v[40:41], v[20:21]
	v_pk_fma_f32 v[18:19], v[116:117], v[120:121], v[18:19]
	v_pk_fma_f32 v[20:21], v[118:119], v[42:43], v[20:21]
	v_pk_fma_f32 v[18:19], v[118:119], v[122:123], v[18:19]
	s_or_b64 exec, exec, s[4:5]
	v_add_f32_e32 v20, v20, v21
	v_mov_b32_e32 v21, 2
	v_lshlrev_b32_sdwa v26, v21, v0 dst_sel:DWORD dst_unused:UNUSED_PAD src0_sel:DWORD src1_sel:BYTE_0
	v_lshl_or_b32 v25, v1, 10, v26
	v_add_f32_e32 v18, v18, v19
	s_movk_i32 s3, 0x100
	ds_write2st64_b32 v25, v20, v18 offset1:16
	v_cmp_gt_u32_e64 s[4:5], s3, v0
	v_lshl_or_b32 v18, s2, 8, v0
	s_waitcnt lgkmcnt(0)
	s_barrier
	s_and_saveexec_b64 s[20:21], s[4:5]
	s_cbranch_execz .LBB12_7
	v_lshl_or_b32 v20, s2, 11, v0
	s_lshl_b32 s2, s2, 13
	s_and_b32 s2, s2, 0xe000
	v_lshl_or_b32 v28, v0, 2, s2
	v_mov_b32_e32 v29, 0
	s_movk_i32 s3, 0x1000
	v_lshl_add_u64 v[30:31], s[12:13], 0, v[28:29]
	v_add_co_u32_e32 v32, vcc, s3, v30
	s_mov_b32 s2, 0x10000
	s_nop 0
	v_addc_co_u32_e32 v33, vcc, 0, v31, vcc
	v_add_co_u32_e32 v34, vcc, s2, v30
	s_mov_b32 s2, 0x11000
	s_nop 0
	v_addc_co_u32_e32 v35, vcc, 0, v31, vcc
	v_add_co_u32_e32 v36, vcc, s2, v30
	s_mov_b32 s2, 0x20000
	s_nop 0
	v_addc_co_u32_e32 v37, vcc, 0, v31, vcc
	v_add_co_u32_e32 v38, vcc, s2, v30
	v_ashrrev_i32_e32 v21, 31, v20
	s_nop 0
	v_addc_co_u32_e32 v39, vcc, 0, v31, vcc
	s_mov_b32 s2, 0x21000
	v_lshl_add_u64 v[20:21], v[20:21], 2, s[12:13]
	v_add_co_u32_e32 v40, vcc, s2, v30
	global_load_dword v19, v[20:21], off
	global_load_dword v27, v[20:21], off offset:1024
	v_addc_co_u32_e32 v41, vcc, 0, v31, vcc
	global_load_dword v42, v[32:33], off
	global_load_dword v43, v[32:33], off offset:1024
	global_load_dword v44, v[32:33], off offset:2048
	global_load_dword v45, v[32:33], off offset:3072
	global_load_dword v46, v[34:35], off offset:1024
	global_load_dword v47, v[34:35], off offset:2048
	global_load_dword v48, v[34:35], off offset:3072
	global_load_dword v49, v[38:39], off offset:1024
	global_load_dword v50, v28, s[12:13]
	global_load_dword v51, v28, s[12:13] offset:1024
	global_load_dword v52, v28, s[12:13] offset:2048
	global_load_dword v53, v[38:39], off offset:2048
	global_load_dword v54, v[38:39], off offset:3072
	global_load_dword v55, v28, s[12:13] offset:3072
	global_load_dword v56, v[36:37], off offset:-4096
	global_load_dword v33, v[36:37], off
	global_load_dword v35, v[36:37], off offset:1024
	s_nop 0
	global_load_dword v38, v[36:37], off offset:2048
	global_load_dword v39, v[36:37], off offset:3072
	global_load_dword v57, v[40:41], off offset:-4096
	global_load_dword v58, v[40:41], off
	s_mov_b32 s2, 0x30000
	v_add_co_u32_e32 v28, vcc, s2, v30
	s_mov_b32 s2, 0x31000
	s_nop 0
	v_addc_co_u32_e32 v29, vcc, 0, v31, vcc
	v_add_co_u32_e32 v30, vcc, s2, v30
	s_waitcnt vmcnt(22)
	v_add_f32_e32 v19, 0, v19
	v_addc_co_u32_e32 v31, vcc, 0, v31, vcc
	global_load_dword v37, v[40:41], off offset:1024
	global_load_dword v59, v[40:41], off offset:2048
	global_load_dword v60, v[40:41], off offset:3072
	global_load_dword v61, v[30:31], off offset:-4096
	global_load_dword v62, v[28:29], off offset:1024
	global_load_dword v63, v[28:29], off offset:2048
	global_load_dword v64, v[28:29], off offset:3072
	global_load_dword v65, v[30:31], off
	v_add_co_u32_e32 v28, vcc, 0x1000, v20
	s_waitcnt vmcnt(29)
	v_add_f32_e32 v19, v19, v27
	v_addc_co_u32_e32 v29, vcc, 0, v21, vcc
	global_load_dword v66, v[20:21], off offset:2048
	global_load_dword v67, v[20:21], off offset:3072
	global_load_dword v68, v[28:29], off
	s_nop 0
	global_load_dword v20, v[28:29], off offset:1024
	global_load_dword v32, v[28:29], off offset:2048
	s_nop 0
	global_load_dword v28, v[28:29], off offset:3072
	s_nop 0
	global_load_dword v29, v26, s[6:7]
	global_load_dword v34, v[30:31], off offset:1024
	global_load_dword v36, v[30:31], off offset:2048
	s_nop 0
	global_load_dword v30, v[30:31], off offset:3072
	s_waitcnt vmcnt(30)
	v_add_f32_e32 v21, 0, v50
	s_waitcnt vmcnt(29)
	v_add_f32_e32 v21, v21, v51
	s_waitcnt vmcnt(28)
	v_add_f32_e32 v21, v21, v52
	s_waitcnt vmcnt(25)
	v_add_f32_e32 v21, v21, v55
	v_add_f32_e32 v21, v21, v42
	v_add_f32_e32 v21, v21, v43
	v_add_f32_e32 v21, v21, v44
	v_add_f32_e32 v21, v21, v45
	s_waitcnt vmcnt(24)
	v_add_f32_e32 v21, v21, v56
	v_add_f32_e32 v21, v21, v46
	v_add_f32_e32 v21, v21, v47
	v_add_f32_e32 v21, v21, v48
	s_waitcnt vmcnt(23)
	v_add_f32_e32 v21, v21, v33
	s_waitcnt vmcnt(22)
	v_add_f32_e32 v21, v21, v35
	s_waitcnt vmcnt(21)
	v_add_f32_e32 v21, v21, v38
	s_waitcnt vmcnt(20)
	v_add_f32_e32 v21, v21, v39
	s_waitcnt vmcnt(19)
	v_add_f32_e32 v21, v21, v57
	v_add_f32_e32 v21, v21, v49
	v_add_f32_e32 v21, v21, v53
	v_add_f32_e32 v21, v21, v54
	s_waitcnt vmcnt(18)
	v_add_f32_e32 v21, v21, v58
	ds_read2st64_b32 v[40:41], v26 offset0:8 offset1:12
	ds_read2st64_b32 v[42:43], v26 offset1:4
	s_waitcnt lgkmcnt(1)
	v_add_f32_e32 v33, v40, v41
	s_waitcnt lgkmcnt(0)
	v_mov_b32_e32 v45, v42
	s_waitcnt vmcnt(17)
	v_add_f32_e32 v21, v21, v37
	s_waitcnt vmcnt(16)
	v_add_f32_e32 v21, v21, v59
	s_waitcnt vmcnt(15)
	v_add_f32_e32 v21, v21, v60
	s_waitcnt vmcnt(14)
	v_add_f32_e32 v21, v21, v61
	s_waitcnt vmcnt(13)
	v_add_f32_e32 v21, v21, v62
	s_waitcnt vmcnt(12)
	v_add_f32_e32 v21, v21, v63
	s_waitcnt vmcnt(11)
	v_add_f32_e32 v21, v21, v64
	s_waitcnt vmcnt(10)
	v_add_f32_e32 v38, v21, v65
	s_waitcnt vmcnt(9)
	v_add_f32_e32 v19, v19, v66
	v_mov_b32_e32 v21, v43
	ds_read2st64_b32 v[40:41], v26 offset0:24 offset1:28
	ds_read2st64_b32 v[42:43], v26 offset0:16 offset1:20
	s_waitcnt vmcnt(8)
	v_add_f32_e32 v19, v19, v67
	s_waitcnt vmcnt(7)
	v_add_f32_e32 v44, v19, v68
	s_waitcnt vmcnt(6)
	v_pk_add_f32 v[20:21], v[44:45], v[20:21]
	s_waitcnt lgkmcnt(1)
	v_add_f32_e32 v37, v40, v41
	s_waitcnt vmcnt(5)
	v_pk_add_f32 v[20:21], v[20:21], v[32:33]
	s_waitcnt lgkmcnt(0)
	v_mov_b32_e32 v39, v42
	s_waitcnt vmcnt(3)
	v_pk_add_f32 v[20:21], v[20:21], v[28:29]
	v_mov_b32_e32 v35, v43
	v_fmamk_f32 v27, v20, 0x3a800000, v21
	s_waitcnt vmcnt(2)
	v_pk_add_f32 v[20:21], v[38:39], v[34:35]
	v_mov_b32_e32 v31, v29
	s_waitcnt vmcnt(1)
	v_pk_add_f32 v[20:21], v[20:21], v[36:37]
	v_ashrrev_i32_e32 v19, 31, v18
	s_waitcnt vmcnt(0)
	v_pk_add_f32 v[20:21], v[20:21], v[30:31]
	s_nop 0
	v_fmamk_f32 v28, v20, 0x39800000, v21
	v_lshl_add_u64 v[20:21], v[18:19], 2, s[14:15]
	global_store_dword v[20:21], v27, off
	ds_write_b32 v26, v28 offset:10240
.LBB12_7:
	s_or_b64 exec, exec, s[20:21]
	v_mov_b32_e32 v20, 0
	v_or_b32_e32 v19, 0x2800, v24
	s_mov_b64 s[2:3], 0
	s_mov_b64 s[12:13], s[10:11]
	v_mov_b32_e32 v24, v22
	v_mov_b32_e32 v21, v20
	s_waitcnt lgkmcnt(0)
	s_barrier
	v_lshl_add_u64 v[26:27], s[12:13], 0, v[8:9]
	v_lshl_add_u64 v[28:29], s[12:13], 0, v[14:15]
	v_lshl_add_u64 v[30:31], s[12:13], 0, v[16:17]
	v_lshl_add_u64 v[32:33], s[12:13], 0, v[12:13]
	v_lshl_add_u64 v[34:35], s[12:13], 0, v[10:11]
	v_lshl_add_u64 v[36:37], s[12:13], 0, v[6:7]
	v_lshl_add_u64 v[38:39], s[12:13], 0, v[4:5]
	v_lshl_add_u64 v[40:41], s[12:13], 0, v[2:3]
	global_load_dword v42, v[26:27], off offset:-1024
	global_load_dword v43, v[26:27], off
	global_load_dword v44, v[28:29], off offset:-1024
	global_load_dword v45, v[28:29], off
	global_load_dword v46, v[30:31], off offset:-1024
	global_load_dword v47, v[30:31], off
	global_load_dword v48, v[32:33], off offset:-1024
	global_load_dword v49, v[32:33], off
	global_load_dword v50, v[34:35], off offset:-1024
	global_load_dword v51, v[34:35], off
	global_load_dword v52, v[36:37], off offset:-1024
	global_load_dword v53, v[36:37], off
	global_load_dword v54, v[38:39], off offset:-1024
	global_load_dword v55, v[38:39], off
	global_load_dword v56, v[40:41], off offset:-1024
	global_load_dword v57, v[40:41], off
	s_add_u32 s12, s12, 0x4000
	s_addc_u32 s13, s13, 0
	v_lshl_add_u64 v[26:27], s[12:13], 0, v[8:9]
	v_lshl_add_u64 v[28:29], s[12:13], 0, v[14:15]
	v_lshl_add_u64 v[30:31], s[12:13], 0, v[16:17]
	v_lshl_add_u64 v[32:33], s[12:13], 0, v[12:13]
	v_lshl_add_u64 v[34:35], s[12:13], 0, v[10:11]
	v_lshl_add_u64 v[36:37], s[12:13], 0, v[6:7]
	v_lshl_add_u64 v[38:39], s[12:13], 0, v[4:5]
	v_lshl_add_u64 v[40:41], s[12:13], 0, v[2:3]
	global_load_dword v72, v[26:27], off offset:-1024
	global_load_dword v73, v[26:27], off
	global_load_dword v74, v[28:29], off offset:-1024
	global_load_dword v75, v[28:29], off
	global_load_dword v76, v[30:31], off offset:-1024
	global_load_dword v77, v[30:31], off
	global_load_dword v78, v[32:33], off offset:-1024
	global_load_dword v79, v[32:33], off
	global_load_dword v80, v[34:35], off offset:-1024
	global_load_dword v81, v[34:35], off
	global_load_dword v82, v[36:37], off offset:-1024
	global_load_dword v83, v[36:37], off
	global_load_dword v84, v[38:39], off offset:-1024
	global_load_dword v85, v[38:39], off
	global_load_dword v86, v[40:41], off offset:-1024
	global_load_dword v87, v[40:41], off
	s_add_u32 s12, s12, 0x4000
	s_addc_u32 s13, s13, 0
	v_lshl_add_u64 v[26:27], s[12:13], 0, v[8:9]
	v_lshl_add_u64 v[28:29], s[12:13], 0, v[14:15]
	v_lshl_add_u64 v[30:31], s[12:13], 0, v[16:17]
	v_lshl_add_u64 v[32:33], s[12:13], 0, v[12:13]
	v_lshl_add_u64 v[34:35], s[12:13], 0, v[10:11]
	v_lshl_add_u64 v[36:37], s[12:13], 0, v[6:7]
	v_lshl_add_u64 v[38:39], s[12:13], 0, v[4:5]
	v_lshl_add_u64 v[40:41], s[12:13], 0, v[2:3]
	global_load_dword v88, v[26:27], off offset:-1024
	global_load_dword v89, v[26:27], off
	global_load_dword v90, v[28:29], off offset:-1024
	global_load_dword v91, v[28:29], off
	global_load_dword v92, v[30:31], off offset:-1024
	global_load_dword v93, v[30:31], off
	global_load_dword v94, v[32:33], off offset:-1024
	global_load_dword v95, v[32:33], off
	global_load_dword v96, v[34:35], off offset:-1024
	global_load_dword v97, v[34:35], off
	global_load_dword v98, v[36:37], off offset:-1024
	global_load_dword v99, v[36:37], off
	global_load_dword v100, v[38:39], off offset:-1024
	global_load_dword v101, v[38:39], off
	global_load_dword v102, v[40:41], off offset:-1024
	global_load_dword v103, v[40:41], off
	s_add_u32 s12, s12, 0x4000
	s_addc_u32 s13, s13, 0
	ds_read_b128 v[26:29], v19 offset:0
	ds_read_b128 v[30:33], v19 offset:16
	ds_read_b128 v[34:37], v19 offset:32
	ds_read_b128 v[38:41], v19 offset:48
	s_waitcnt vmcnt(32) lgkmcnt(0)
	v_pk_fma_f32 v[20:21], v[42:43], v[26:27], v[20:21]
	v_pk_fma_f32 v[20:21], v[44:45], v[28:29], v[20:21]
	v_pk_fma_f32 v[20:21], v[46:47], v[30:31], v[20:21]
	v_pk_fma_f32 v[20:21], v[48:49], v[32:33], v[20:21]
	v_pk_fma_f32 v[20:21], v[50:51], v[34:35], v[20:21]
	v_pk_fma_f32 v[20:21], v[52:53], v[36:37], v[20:21]
	v_pk_fma_f32 v[20:21], v[54:55], v[38:39], v[20:21]
	v_pk_fma_f32 v[20:21], v[56:57], v[40:41], v[20:21]
	v_lshl_add_u64 v[26:27], s[12:13], 0, v[8:9]
	v_lshl_add_u64 v[28:29], s[12:13], 0, v[14:15]
	v_lshl_add_u64 v[30:31], s[12:13], 0, v[16:17]
	v_lshl_add_u64 v[32:33], s[12:13], 0, v[12:13]
	v_lshl_add_u64 v[34:35], s[12:13], 0, v[10:11]
	v_lshl_add_u64 v[36:37], s[12:13], 0, v[6:7]
	v_lshl_add_u64 v[38:39], s[12:13], 0, v[4:5]
	v_lshl_add_u64 v[40:41], s[12:13], 0, v[2:3]
	global_load_dword v104, v[26:27], off offset:-1024
	global_load_dword v105, v[26:27], off
	global_load_dword v106, v[28:29], off offset:-1024
	global_load_dword v107, v[28:29], off
	global_load_dword v108, v[30:31], off offset:-1024
	global_load_dword v109, v[30:31], off
	global_load_dword v110, v[32:33], off offset:-1024
	global_load_dword v111, v[32:33], off
	global_load_dword v112, v[34:35], off offset:-1024
	global_load_dword v113, v[34:35], off
	global_load_dword v114, v[36:37], off offset:-1024
	global_load_dword v115, v[36:37], off
	global_load_dword v116, v[38:39], off offset:-1024
	global_load_dword v117, v[38:39], off
	global_load_dword v118, v[40:41], off offset:-1024
	global_load_dword v119, v[40:41], off
	s_add_u32 s12, s12, 0x4000
	s_addc_u32 s13, s13, 0
	ds_read_b128 v[26:29], v19 offset:64
	ds_read_b128 v[30:33], v19 offset:80
	ds_read_b128 v[34:37], v19 offset:96
	ds_read_b128 v[38:41], v19 offset:112
	s_waitcnt vmcnt(32) lgkmcnt(0)
	v_pk_fma_f32 v[20:21], v[72:73], v[26:27], v[20:21]
	v_pk_fma_f32 v[20:21], v[74:75], v[28:29], v[20:21]
	v_pk_fma_f32 v[20:21], v[76:77], v[30:31], v[20:21]
	v_pk_fma_f32 v[20:21], v[78:79], v[32:33], v[20:21]
	v_pk_fma_f32 v[20:21], v[80:81], v[34:35], v[20:21]
	v_pk_fma_f32 v[20:21], v[82:83], v[36:37], v[20:21]
	v_pk_fma_f32 v[20:21], v[84:85], v[38:39], v[20:21]
	v_pk_fma_f32 v[20:21], v[86:87], v[40:41], v[20:21]
	ds_read_b128 v[26:29], v19 offset:128
	ds_read_b128 v[30:33], v19 offset:144
	ds_read_b128 v[34:37], v19 offset:160
	ds_read_b128 v[38:41], v19 offset:176
	s_waitcnt vmcnt(16) lgkmcnt(0)
	v_pk_fma_f32 v[20:21], v[88:89], v[26:27], v[20:21]
	v_pk_fma_f32 v[20:21], v[90:91], v[28:29], v[20:21]
	v_pk_fma_f32 v[20:21], v[92:93], v[30:31], v[20:21]
	v_pk_fma_f32 v[20:21], v[94:95], v[32:33], v[20:21]
	v_pk_fma_f32 v[20:21], v[96:97], v[34:35], v[20:21]
	v_pk_fma_f32 v[20:21], v[98:99], v[36:37], v[20:21]
	v_pk_fma_f32 v[20:21], v[100:101], v[38:39], v[20:21]
	v_pk_fma_f32 v[20:21], v[102:103], v[40:41], v[20:21]
	ds_read_b128 v[26:29], v19 offset:192
	ds_read_b128 v[30:33], v19 offset:208
	ds_read_b128 v[34:37], v19 offset:224
	ds_read_b128 v[38:41], v19 offset:240
	s_waitcnt vmcnt(0) lgkmcnt(0)
	v_pk_fma_f32 v[20:21], v[104:105], v[26:27], v[20:21]
	v_pk_fma_f32 v[20:21], v[106:107], v[28:29], v[20:21]
	v_pk_fma_f32 v[20:21], v[108:109], v[30:31], v[20:21]
	v_pk_fma_f32 v[20:21], v[110:111], v[32:33], v[20:21]
	v_pk_fma_f32 v[20:21], v[112:113], v[34:35], v[20:21]
	v_pk_fma_f32 v[20:21], v[114:115], v[36:37], v[20:21]
	v_pk_fma_f32 v[20:21], v[116:117], v[38:39], v[20:21]
	v_pk_fma_f32 v[20:21], v[118:119], v[40:41], v[20:21]
	s_or_b64 exec, exec, s[2:3]
	v_add_f32_e32 v2, v20, v21
	ds_write_b32 v25, v2
	s_waitcnt lgkmcnt(0)
	s_barrier
	s_and_saveexec_b64 s[2:3], s[4:5]
	s_cbranch_execz .LBB12_11
	v_mov_b32_e32 v2, 2
	v_lshlrev_b32_sdwa v4, v2, v0 dst_sel:DWORD dst_unused:UNUSED_PAD src0_sel:DWORD src1_sel:BYTE_0
	ds_read2st64_b32 v[2:3], v4 offset1:4
	ds_read2st64_b32 v[4:5], v4 offset0:8 offset1:12
	v_ashrrev_i32_e32 v19, 31, v18
	s_waitcnt lgkmcnt(1)
	v_mov_b32_e32 v6, v2
	s_waitcnt lgkmcnt(0)
	v_mov_b32_e32 v7, v4
	v_mov_b32_e32 v4, v3
	v_pk_add_f32 v[2:3], v[6:7], v[4:5]
	s_nop 0
	v_add_f32_e32 v4, v2, v3
	v_lshl_add_u64 v[2:3], v[18:19], 2, s[18:19]
	global_store_dword v[2:3], v4, off

.LBB12_12:
	s_and_b64 vcc, exec, s[4:5]
	s_cbranch_vccz .LBB12_23
	s_load_dwordx2 s[4:5], s[0:1], 0x48
	s_load_dwordx2 s[2:3], s[0:1], 0x38
	v_lshlrev_b32_e32 v2, 14, v1
	v_or_b32_e32 v3, v0, v2
	v_or_b32_sdwa v2, v2, v0 dst_sel:DWORD dst_unused:UNUSED_PAD src0_sel:DWORD src1_sel:BYTE_0
	v_lshlrev_b32_e32 v2, 2, v2
	v_mov_b32_e32 v5, 0
	v_lshlrev_b32_e32 v16, 2, v3
	v_add_u32_e32 v23, 64, v22
	v_or_b32_e32 v4, 0x3000, v2
	v_or_b32_e32 v8, 0x3c00, v16
	v_mov_b32_e32 v9, v5
	v_or_b32_e32 v10, 0x2000, v2
	v_mov_b32_e32 v11, v5
	v_mov_b32_e32 v3, v5
	v_or_b32_e32 v12, 0x2c00, v16
	v_mov_b32_e32 v13, v5
	v_or_b32_e32 v6, 0x1000, v2
	v_mov_b32_e32 v7, v5
	v_or_b32_e32 v14, 0x1c00, v16
	v_mov_b32_e32 v15, v5
	v_or_b32_e32 v16, 0xc00, v16
	v_mov_b32_e32 v17, v5
	s_mov_b64 s[0:1], 0
	v_mov_b32_e32 v24, v22
	v_mov_b32_e32 v18, v5
	v_mov_b32_e32 v19, v5
	v_mov_b32_e32 v20, v5
	v_mov_b32_e32 v21, v5
	s_waitcnt lgkmcnt(0)
	v_lshl_add_u64 v[26:27], s[10:11], 0, v[2:3]
	v_lshl_add_u64 v[28:29], s[10:11], 0, v[16:17]
	v_lshl_add_u64 v[30:31], s[10:11], 0, v[6:7]
	v_lshl_add_u64 v[32:33], s[10:11], 0, v[14:15]
	v_lshl_add_u64 v[34:35], s[10:11], 0, v[10:11]
	v_lshl_add_u64 v[36:37], s[10:11], 0, v[12:13]
	v_lshl_add_u64 v[38:39], s[10:11], 0, v[4:5]
	v_lshl_add_u64 v[40:41], s[10:11], 0, v[8:9]
	global_load_dword v43, v[26:27], off
	global_load_dword v45, v[26:27], off offset:1024
	global_load_dword v44, v[26:27], off offset:2048
	global_load_dword v42, v[28:29], off
	global_load_dword v47, v[30:31], off
	global_load_dword v49, v[30:31], off offset:1024
	global_load_dword v48, v[30:31], off offset:2048
	global_load_dword v46, v[32:33], off
	global_load_dword v51, v[34:35], off
	global_load_dword v53, v[34:35], off offset:1024
	global_load_dword v52, v[34:35], off offset:2048
	global_load_dword v50, v[36:37], off
	global_load_dword v55, v[38:39], off
	global_load_dword v57, v[38:39], off offset:1024
	global_load_dword v56, v[38:39], off offset:2048
	global_load_dword v54, v[40:41], off
	s_add_u32 s10, s10, 0x4000
	s_addc_u32 s11, s11, 0
	v_lshl_add_u64 v[26:27], s[10:11], 0, v[2:3]
	v_lshl_add_u64 v[28:29], s[10:11], 0, v[16:17]
	v_lshl_add_u64 v[30:31], s[10:11], 0, v[6:7]
	v_lshl_add_u64 v[32:33], s[10:11], 0, v[14:15]
	v_lshl_add_u64 v[34:35], s[10:11], 0, v[10:11]
	v_lshl_add_u64 v[36:37], s[10:11], 0, v[12:13]
	v_lshl_add_u64 v[38:39], s[10:11], 0, v[4:5]
	v_lshl_add_u64 v[40:41], s[10:11], 0, v[8:9]
	global_load_dword v73, v[26:27], off
	global_load_dword v75, v[26:27], off offset:1024
	global_load_dword v74, v[26:27], off offset:2048
	global_load_dword v72, v[28:29], off
	global_load_dword v77, v[30:31], off
	global_load_dword v79, v[30:31], off offset:1024
	global_load_dword v78, v[30:31], off offset:2048
	global_load_dword v76, v[32:33], off
	global_load_dword v81, v[34:35], off
	global_load_dword v83, v[34:35], off offset:1024
	global_load_dword v82, v[34:35], off offset:2048
	global_load_dword v80, v[36:37], off
	global_load_dword v85, v[38:39], off
	global_load_dword v87, v[38:39], off offset:1024
	global_load_dword v86, v[38:39], off offset:2048
	global_load_dword v84, v[40:41], off
	s_add_u32 s10, s10, 0x4000
	s_addc_u32 s11, s11, 0
	v_lshl_add_u64 v[26:27], s[10:11], 0, v[2:3]
	v_lshl_add_u64 v[28:29], s[10:11], 0, v[16:17]
	v_lshl_add_u64 v[30:31], s[10:11], 0, v[6:7]
	v_lshl_add_u64 v[32:33], s[10:11], 0, v[14:15]
	v_lshl_add_u64 v[34:35], s[10:11], 0, v[10:11]
	v_lshl_add_u64 v[36:37], s[10:11], 0, v[12:13]
	v_lshl_add_u64 v[38:39], s[10:11], 0, v[4:5]
	v_lshl_add_u64 v[40:41], s[10:11], 0, v[8:9]
	global_load_dword v89, v[26:27], off
	global_load_dword v91, v[26:27], off offset:1024
	global_load_dword v90, v[26:27], off offset:2048
	global_load_dword v88, v[28:29], off
	global_load_dword v93, v[30:31], off
	global_load_dword v95, v[30:31], off offset:1024
	global_load_dword v94, v[30:31], off offset:2048
	global_load_dword v92, v[32:33], off
	global_load_dword v97, v[34:35], off
	global_load_dword v99, v[34:35], off offset:1024
	global_load_dword v98, v[34:35], off offset:2048
	global_load_dword v96, v[36:37], off
	global_load_dword v101, v[38:39], off
	global_load_dword v103, v[38:39], off offset:1024
	global_load_dword v102, v[38:39], off offset:2048
	global_load_dword v100, v[40:41], off
	s_add_u32 s10, s10, 0x4000
	s_addc_u32 s11, s11, 0
	s_waitcnt vmcnt(32)
	v_pk_add_f32 v[18:19], v[18:19], v[44:45]
	v_pk_add_f32 v[20:21], v[20:21], v[42:43]
	v_pk_add_f32 v[18:19], v[18:19], v[48:49]
	v_pk_add_f32 v[20:21], v[20:21], v[46:47]
	v_pk_add_f32 v[18:19], v[18:19], v[52:53]
	v_pk_add_f32 v[20:21], v[20:21], v[50:51]
	v_pk_add_f32 v[18:19], v[18:19], v[56:57]
	v_pk_add_f32 v[20:21], v[20:21], v[54:55]
	v_lshl_add_u64 v[26:27], s[10:11], 0, v[2:3]
	v_lshl_add_u64 v[28:29], s[10:11], 0, v[16:17]
	v_lshl_add_u64 v[30:31], s[10:11], 0, v[6:7]
	v_lshl_add_u64 v[32:33], s[10:11], 0, v[14:15]
	v_lshl_add_u64 v[34:35], s[10:11], 0, v[10:11]
	v_lshl_add_u64 v[36:37], s[10:11], 0, v[12:13]
	v_lshl_add_u64 v[38:39], s[10:11], 0, v[4:5]
	v_lshl_add_u64 v[40:41], s[10:11], 0, v[8:9]
	global_load_dword v105, v[26:27], off
	global_load_dword v107, v[26:27], off offset:1024
	global_load_dword v106, v[26:27], off offset:2048
	global_load_dword v104, v[28:29], off
	global_load_dword v109, v[30:31], off
	global_load_dword v111, v[30:31], off offset:1024
	global_load_dword v110, v[30:31], off offset:2048
	global_load_dword v108, v[32:33], off
	global_load_dword v113, v[34:35], off
	global_load_dword v115, v[34:35], off offset:1024
	global_load_dword v114, v[34:35], off offset:2048
	global_load_dword v112, v[36:37], off
	global_load_dword v117, v[38:39], off
	global_load_dword v119, v[38:39], off offset:1024
	global_load_dword v118, v[38:39], off offset:2048
	global_load_dword v116, v[40:41], off
	s_add_u32 s10, s10, 0x4000
	s_addc_u32 s11, s11, 0
	s_waitcnt vmcnt(32)
	v_pk_add_f32 v[18:19], v[18:19], v[74:75]
	v_pk_add_f32 v[20:21], v[20:21], v[72:73]
	v_pk_add_f32 v[18:19], v[18:19], v[78:79]
	v_pk_add_f32 v[20:21], v[20:21], v[76:77]
	v_pk_add_f32 v[18:19], v[18:19], v[82:83]
	v_pk_add_f32 v[20:21], v[20:21], v[80:81]
	v_pk_add_f32 v[18:19], v[18:19], v[86:87]
	v_pk_add_f32 v[20:21], v[20:21], v[84:85]
	s_waitcnt vmcnt(16)
	v_pk_add_f32 v[18:19], v[18:19], v[90:91]
	v_pk_add_f32 v[20:21], v[20:21], v[88:89]
	v_pk_add_f32 v[18:19], v[18:19], v[94:95]
	v_pk_add_f32 v[20:21], v[20:21], v[92:93]
	v_pk_add_f32 v[18:19], v[18:19], v[98:99]
	v_pk_add_f32 v[20:21], v[20:21], v[96:97]
	v_pk_add_f32 v[18:19], v[18:19], v[102:103]
	v_pk_add_f32 v[20:21], v[20:21], v[100:101]
	s_waitcnt vmcnt(0)
	v_pk_add_f32 v[18:19], v[18:19], v[106:107]
	v_pk_add_f32 v[20:21], v[20:21], v[104:105]
	v_pk_add_f32 v[18:19], v[18:19], v[110:111]
	v_pk_add_f32 v[20:21], v[20:21], v[108:109]
	v_pk_add_f32 v[18:19], v[18:19], v[114:115]
	v_pk_add_f32 v[20:21], v[20:21], v[112:113]
	v_pk_add_f32 v[18:19], v[18:19], v[118:119]
	v_pk_add_f32 v[20:21], v[20:21], v[116:117]
	s_or_b64 exec, exec, s[0:1]
	v_pk_add_f32 v[4:5], v[18:19], v[20:21]
	s_mov_b64 s[0:1], 0x400
	v_add_f32_e32 v4, v4, v5
	v_mov_b32_e32 v5, 2
	v_lshlrev_b32_sdwa v5, v5, v0 dst_sel:DWORD dst_unused:UNUSED_PAD src0_sel:DWORD src1_sel:BYTE_0
	v_lshl_or_b32 v14, v1, 10, v5
	ds_write_b32 v14, v4
	v_add_u32_e32 v4, 0x1800, v2
	v_mov_b32_e32 v5, 0
	v_lshl_add_u64 v[8:9], v[4:5], 0, s[0:1]
	v_add_u32_e32 v4, 0x800, v2
	v_lshl_add_u64 v[10:11], v[2:3], 0, s[0:1]
	v_lshl_add_u64 v[2:3], v[4:5], 0, s[0:1]
	v_and_b32_e32 v4, 0x300, v0
	v_lshl_add_u64 v[12:13], s[16:17], 0, v[4:5]
	v_lshl_add_u64 v[6:7], v[6:7], 0, s[0:1]
	v_lshl_add_u64 v[12:13], v[12:13], 0, 16
	s_mov_b64 s[0:1], 0
	v_mov_b32_e32 v4, v5
	global_load_dwordx4 v[64:67], v[12:13], off
	global_load_dwordx4 v[60:63], v[12:13], off offset:-16
	v_lshl_add_u64 v[20:21], s[8:9], 0, v[10:11]
	v_lshl_add_u64 v[28:29], s[8:9], 0, v[2:3]
	v_lshl_add_u64 v[30:31], s[8:9], 0, v[6:7]
	v_lshl_add_u64 v[32:33], s[8:9], 0, v[8:9]
	global_load_dword v68, v[20:21], off offset:-1024
	global_load_dword v69, v[20:21], off
	global_load_dword v70, v[28:29], off offset:-1024
	global_load_dword v71, v[28:29], off
	global_load_dword v72, v[30:31], off offset:-1024
	global_load_dword v73, v[30:31], off
	global_load_dword v74, v[32:33], off offset:-1024
	global_load_dword v75, v[32:33], off
	s_add_u32 s8, s8, 0x2000
	s_addc_u32 s9, s9, 0
	v_lshl_add_u64 v[12:13], v[12:13], 0, 32
	global_load_dwordx4 v[80:83], v[12:13], off
	global_load_dwordx4 v[76:79], v[12:13], off offset:-16
	v_lshl_add_u64 v[20:21], s[8:9], 0, v[10:11]
	v_lshl_add_u64 v[28:29], s[8:9], 0, v[2:3]
	v_lshl_add_u64 v[30:31], s[8:9], 0, v[6:7]
	v_lshl_add_u64 v[32:33], s[8:9], 0, v[8:9]
	global_load_dword v84, v[20:21], off offset:-1024
	global_load_dword v85, v[20:21], off
	global_load_dword v86, v[28:29], off offset:-1024
	global_load_dword v87, v[28:29], off
	global_load_dword v88, v[30:31], off offset:-1024
	global_load_dword v89, v[30:31], off
	global_load_dword v90, v[32:33], off offset:-1024
	global_load_dword v91, v[32:33], off
	s_add_u32 s8, s8, 0x2000
	s_addc_u32 s9, s9, 0
	v_lshl_add_u64 v[12:13], v[12:13], 0, 32
	global_load_dwordx4 v[96:99], v[12:13], off
	global_load_dwordx4 v[92:95], v[12:13], off offset:-16
	v_lshl_add_u64 v[20:21], s[8:9], 0, v[10:11]
	v_lshl_add_u64 v[28:29], s[8:9], 0, v[2:3]
	v_lshl_add_u64 v[30:31], s[8:9], 0, v[6:7]
	v_lshl_add_u64 v[32:33], s[8:9], 0, v[8:9]
	global_load_dword v100, v[20:21], off offset:-1024
	global_load_dword v101, v[20:21], off
	global_load_dword v102, v[28:29], off offset:-1024
	global_load_dword v103, v[28:29], off
	global_load_dword v104, v[30:31], off offset:-1024
	global_load_dword v105, v[30:31], off
	global_load_dword v106, v[32:33], off offset:-1024
	global_load_dword v107, v[32:33], off
	s_add_u32 s8, s8, 0x2000
	s_addc_u32 s9, s9, 0
	v_lshl_add_u64 v[12:13], v[12:13], 0, 32
	global_load_dwordx4 v[112:115], v[12:13], off
	global_load_dwordx4 v[108:111], v[12:13], off offset:-16
	v_lshl_add_u64 v[20:21], s[8:9], 0, v[10:11]
	v_lshl_add_u64 v[28:29], s[8:9], 0, v[2:3]
	v_lshl_add_u64 v[30:31], s[8:9], 0, v[6:7]
	v_lshl_add_u64 v[32:33], s[8:9], 0, v[8:9]
	global_load_dword v116, v[20:21], off offset:-1024
	global_load_dword v117, v[20:21], off
	global_load_dword v118, v[28:29], off offset:-1024
	global_load_dword v119, v[28:29], off
	global_load_dword v120, v[30:31], off offset:-1024
	global_load_dword v121, v[30:31], off
	global_load_dword v122, v[32:33], off offset:-1024
	global_load_dword v123, v[32:33], off
	s_add_u32 s8, s8, 0x2000
	s_addc_u32 s9, s9, 0
	v_lshl_add_u64 v[12:13], v[12:13], 0, 32
	s_waitcnt vmcnt(30)
	v_pk_fma_f32 v[4:5], v[60:61], v[68:69], v[4:5]
	v_pk_fma_f32 v[4:5], v[62:63], v[70:71], v[4:5]
	v_pk_fma_f32 v[4:5], v[64:65], v[72:73], v[4:5]
	v_pk_fma_f32 v[4:5], v[66:67], v[74:75], v[4:5]
	global_load_dwordx4 v[64:67], v[12:13], off
	global_load_dwordx4 v[60:63], v[12:13], off offset:-16
	v_lshl_add_u64 v[20:21], s[8:9], 0, v[10:11]
	v_lshl_add_u64 v[28:29], s[8:9], 0, v[2:3]
	v_lshl_add_u64 v[30:31], s[8:9], 0, v[6:7]
	v_lshl_add_u64 v[32:33], s[8:9], 0, v[8:9]
	global_load_dword v68, v[20:21], off offset:-1024
	global_load_dword v69, v[20:21], off
	global_load_dword v70, v[28:29], off offset:-1024
	global_load_dword v71, v[28:29], off
	global_load_dword v72, v[30:31], off offset:-1024
	global_load_dword v73, v[30:31], off
	global_load_dword v74, v[32:33], off offset:-1024
	global_load_dword v75, v[32:33], off
	s_add_u32 s8, s8, 0x2000
	s_addc_u32 s9, s9, 0
	v_lshl_add_u64 v[12:13], v[12:13], 0, 32
	s_waitcnt vmcnt(30)
	v_pk_fma_f32 v[4:5], v[76:77], v[84:85], v[4:5]
	v_pk_fma_f32 v[4:5], v[78:79], v[86:87], v[4:5]
	v_pk_fma_f32 v[4:5], v[80:81], v[88:89], v[4:5]
	v_pk_fma_f32 v[4:5], v[82:83], v[90:91], v[4:5]
	global_load_dwordx4 v[80:83], v[12:13], off
	global_load_dwordx4 v[76:79], v[12:13], off offset:-16
	v_lshl_add_u64 v[20:21], s[8:9], 0, v[10:11]
	v_lshl_add_u64 v[28:29], s[8:9], 0, v[2:3]
	v_lshl_add_u64 v[30:31], s[8:9], 0, v[6:7]
	v_lshl_add_u64 v[32:33], s[8:9], 0, v[8:9]
	global_load_dword v84, v[20:21], off offset:-1024
	global_load_dword v85, v[20:21], off
	global_load_dword v86, v[28:29], off offset:-1024
	global_load_dword v87, v[28:29], off
	global_load_dword v88, v[30:31], off offset:-1024
	global_load_dword v89, v[30:31], off
	global_load_dword v90, v[32:33], off offset:-1024
	global_load_dword v91, v[32:33], off
	s_add_u32 s8, s8, 0x2000
	s_addc_u32 s9, s9, 0
	v_lshl_add_u64 v[12:13], v[12:13], 0, 32
	s_waitcnt vmcnt(30)
	v_pk_fma_f32 v[4:5], v[92:93], v[100:101], v[4:5]
	v_pk_fma_f32 v[4:5], v[94:95], v[102:103], v[4:5]
	v_pk_fma_f32 v[4:5], v[96:97], v[104:105], v[4:5]
	v_pk_fma_f32 v[4:5], v[98:99], v[106:107], v[4:5]
	global_load_dwordx4 v[96:99], v[12:13], off
	global_load_dwordx4 v[92:95], v[12:13], off offset:-16
	v_lshl_add_u64 v[20:21], s[8:9], 0, v[10:11]
	v_lshl_add_u64 v[28:29], s[8:9], 0, v[2:3]
	v_lshl_add_u64 v[30:31], s[8:9], 0, v[6:7]
	v_lshl_add_u64 v[32:33], s[8:9], 0, v[8:9]
	global_load_dword v100, v[20:21], off offset:-1024
	global_load_dword v101, v[20:21], off
	global_load_dword v102, v[28:29], off offset:-1024
	global_load_dword v103, v[28:29], off
	global_load_dword v104, v[30:31], off offset:-1024
	global_load_dword v105, v[30:31], off
	global_load_dword v106, v[32:33], off offset:-1024
	global_load_dword v107, v[32:33], off
	s_add_u32 s8, s8, 0x2000
	s_addc_u32 s9, s9, 0
	v_lshl_add_u64 v[12:13], v[12:13], 0, 32
	s_waitcnt vmcnt(30)
	v_pk_fma_f32 v[4:5], v[108:109], v[116:117], v[4:5]
	v_pk_fma_f32 v[4:5], v[110:111], v[118:119], v[4:5]
	v_pk_fma_f32 v[4:5], v[112:113], v[120:121], v[4:5]
	v_pk_fma_f32 v[4:5], v[114:115], v[122:123], v[4:5]
	global_load_dwordx4 v[112:115], v[12:13], off
	global_load_dwordx4 v[108:111], v[12:13], off offset:-16
	v_lshl_add_u64 v[20:21], s[8:9], 0, v[10:11]
	v_lshl_add_u64 v[28:29], s[8:9], 0, v[2:3]
	v_lshl_add_u64 v[30:31], s[8:9], 0, v[6:7]
	v_lshl_add_u64 v[32:33], s[8:9], 0, v[8:9]
	global_load_dword v116, v[20:21], off offset:-1024
	global_load_dword v117, v[20:21], off
	global_load_dword v118, v[28:29], off offset:-1024
	global_load_dword v119, v[28:29], off
	global_load_dword v120, v[30:31], off offset:-1024
	global_load_dword v121, v[30:31], off
	global_load_dword v122, v[32:33], off offset:-1024
	global_load_dword v123, v[32:33], off
	s_add_u32 s8, s8, 0x2000
	s_addc_u32 s9, s9, 0
	v_lshl_add_u64 v[12:13], v[12:13], 0, 32
	s_waitcnt vmcnt(30)
	v_pk_fma_f32 v[4:5], v[60:61], v[68:69], v[4:5]
	v_pk_fma_f32 v[4:5], v[62:63], v[70:71], v[4:5]
	v_pk_fma_f32 v[4:5], v[64:65], v[72:73], v[4:5]
	v_pk_fma_f32 v[4:5], v[66:67], v[74:75], v[4:5]
	s_waitcnt vmcnt(20)
	v_pk_fma_f32 v[4:5], v[76:77], v[84:85], v[4:5]
	v_pk_fma_f32 v[4:5], v[78:79], v[86:87], v[4:5]
	v_pk_fma_f32 v[4:5], v[80:81], v[88:89], v[4:5]
	v_pk_fma_f32 v[4:5], v[82:83], v[90:91], v[4:5]
	s_waitcnt vmcnt(10)
	v_pk_fma_f32 v[4:5], v[92:93], v[100:101], v[4:5]
	v_pk_fma_f32 v[4:5], v[94:95], v[102:103], v[4:5]
	v_pk_fma_f32 v[4:5], v[96:97], v[104:105], v[4:5]
	v_pk_fma_f32 v[4:5], v[98:99], v[106:107], v[4:5]
	s_waitcnt vmcnt(0)
	v_pk_fma_f32 v[4:5], v[108:109], v[116:117], v[4:5]
	v_pk_fma_f32 v[4:5], v[110:111], v[118:119], v[4:5]
	v_pk_fma_f32 v[4:5], v[112:113], v[120:121], v[4:5]
	v_pk_fma_f32 v[4:5], v[114:115], v[122:123], v[4:5]
	s_or_b64 exec, exec, s[0:1]
	s_movk_i32 s0, 0xff
	v_add_f32_e32 v2, v4, v5
	v_cmp_lt_u32_e32 vcc, s0, v0
	ds_write_b32 v14, v2 offset:4096
	s_waitcnt lgkmcnt(0)
	s_barrier
	s_and_saveexec_b64 s[0:1], vcc
	s_xor_b64 s[0:1], exec, s[0:1]
	s_cbranch_execz .LBB12_21
	v_cmp_eq_u32_e32 vcc, 1, v1
	s_and_saveexec_b64 s[8:9], vcc
	s_cbranch_execz .LBB12_20
	v_mov_b32_e32 v1, 2
	v_lshlrev_b32_sdwa v6, v1, v0 dst_sel:DWORD dst_unused:UNUSED_PAD src0_sel:DWORD src1_sel:BYTE_0
	global_load_dword v7, v6, s[6:7]
	ds_read2st64_b32 v[0:1], v6 offset0:16 offset1:20
	ds_read2st64_b32 v[2:3], v6 offset0:24 offset1:28
	s_waitcnt lgkmcnt(1)
	v_mov_b32_e32 v4, v0
	s_waitcnt lgkmcnt(0)
	v_mov_b32_e32 v5, v2
	v_mov_b32_e32 v2, v1
	v_pk_add_f32 v[0:1], v[4:5], v[2:3]
	s_waitcnt vmcnt(0)
	v_add_f32_e32 v0, v7, v0
	v_add_f32_e32 v0, v0, v1
	global_store_dword v6, v0, s[4:5]

	.amdhsa_kernel _Z14special_kernelPKtPKfS2_S2_S2_PfS3_S3_S2_S3_
		.amdhsa_group_segment_fixed_size 11264
		.amdhsa_private_segment_fixed_size 0
		.amdhsa_kernarg_size 80
		.amdhsa_user_sgpr_count 2
		.amdhsa_user_sgpr_dispatch_ptr 0
		.amdhsa_user_sgpr_queue_ptr 0
		.amdhsa_user_sgpr_kernarg_segment_ptr 1
		.amdhsa_user_sgpr_dispatch_id 0
		.amdhsa_user_sgpr_kernarg_preload_length 0
		.amdhsa_user_sgpr_kernarg_preload_offset 0
		.amdhsa_user_sgpr_private_segment_size 0
		.amdhsa_uses_dynamic_stack 0
		.amdhsa_enable_private_segment 0
		.amdhsa_system_sgpr_workgroup_id_x 1
		.amdhsa_system_sgpr_workgroup_id_y 0
		.amdhsa_system_sgpr_workgroup_id_z 0
		.amdhsa_system_sgpr_workgroup_info 0
		.amdhsa_system_vgpr_workitem_id 0
		.amdhsa_next_free_vgpr 124
		.amdhsa_next_free_sgpr 23
		.amdhsa_accum_offset 124
		.amdhsa_reserve_vcc 1
		.amdhsa_float_round_mode_32 0
		.amdhsa_float_round_mode_16_64 0
		.amdhsa_float_denorm_mode_32 3
		.amdhsa_float_denorm_mode_16_64 3
		.amdhsa_dx10_clamp 1
		.amdhsa_ieee_mode 1
		.amdhsa_fp16_overflow 0
		.amdhsa_tg_split 0
		.amdhsa_exception_fp_ieee_invalid_op 0
		.amdhsa_exception_fp_denorm_src 0
		.amdhsa_exception_fp_ieee_div_zero 0
		.amdhsa_exception_fp_ieee_overflow 0
		.amdhsa_exception_fp_ieee_underflow 0
		.amdhsa_exception_fp_ieee_inexact 0
		.amdhsa_exception_int_div_zero 0
	.end_amdhsa_kernel
